# on top of v43: FoX tile loop reads the 8 per-wave early-exit flags with two ds_read_b128 instead of hipcc's chain of 8 dependent ds_read_b32 round trips
# baseline (speedup 1.0000x reference)
; template <int D, bool MASK, bool BIAS, bool SINK, bool REV, bool O8, class BG>
; __device__ __forceinline__ void attn_unit(const Prm& P, LAS unsigned char* lds, BG& bg) {
;     ...
;         if (k != 0 && bg.inflight()) asm volatile("s_waitcnt vmcnt(16)" ::: "memory");
;         else asm volatile("s_waitcnt vmcnt(0)" ::: "memory");
;         __syncthreads();
;         bool more = k + 1 < NT;
;         if (REV && more && k >= 1) { int any = 0;
; #pragma unroll
;             for (int w = 0; w < 8; ++w) any |= nflag[((k - 1) & 1) * 8 + w];
;             more = any != 0; }
.LBB0_437:
	s_add_i32 s56, s57, 1
	s_cmp_lt_u32 s56, s43
	s_cselect_b64 s[96:97], -1, 0
	s_and_b64 s[6:7], s[6:7], s[96:97]
	s_andn2_b64 vcc, exec, s[6:7]
	s_barrier
	s_cbranch_vccnz .LBB0_439
	s_lshl_b32 s6, s57, 3
	s_and_b32 s6, s6, 8
	s_xor_b32 s6, s6, 8
	s_add_i32 s11, 0, 0x10800
	s_lshl_b32 s6, s6, 2
	s_add_i32 s6, s11, s6
	v_mov_b32_e32 v240, s6
	ds_read_b128 v[244:247], v240
	ds_read_b128 v[248:251], v240 offset:16
	s_waitcnt lgkmcnt(0)
	v_or3_b32 v2, v244, v245, v246
	v_or3_b32 v36, v247, v248, v249
	v_or3_b32 v2, v2, v250, v251
	v_or_b32_e32 v2, v2, v36
	v_cmp_ne_u32_e64 s[96:97], 0, v2
